# diff-attention lambda: two 64-element dot products done lane-parallel (4 coalesced loads + wave sum) instead of an 8-iteration load-wait-fma loop in front of the attention units
# speedup vs baseline: 1.0028x; 1.0028x over previous
.LBB0_555:
	s_or_b64 exec, exec, s[0:1]
	s_load_dwordx8 s[12:19], s[2:3], 0x20
	s_lshl_b32 s0, s4, 6
	s_ashr_i32 s1, s0, 31
	s_lshl_b64 s[0:1], s[0:1], 2
	v_mov_b32_e32 v1, 0
	s_waitcnt lgkmcnt(0)
	s_add_u32 s5, s12, s0
	s_addc_u32 s8, s13, s1
	s_add_u32 s9, s18, s0
	s_addc_u32 s10, s19, s1
	s_add_u32 s11, s14, s0
	s_addc_u32 s12, s15, s1
	s_add_u32 s13, s16, s0
	s_addc_u32 s14, s17, s1
	s_mov_b64 s[0:1], 0
	v_mov_b32_e32 v0, 0
	v_and_b32_e32 v2, 63, v231
	v_lshlrev_b32_e32 v2, 2, v2
	s_mov_b32 s16, s5
	s_mov_b32 s17, s8
	global_load_dword v3, v2, s[16:17]
	s_mov_b32 s16, s11
	s_mov_b32 s17, s12
	global_load_dword v4, v2, s[16:17]
	s_mov_b32 s16, s13
	s_mov_b32 s17, s14
	global_load_dword v5, v2, s[16:17]
	s_mov_b32 s16, s9
	s_mov_b32 s17, s10
	global_load_dword v6, v2, s[16:17]
	s_movk_i32 s0, 0x100
	s_waitcnt vmcnt(0)
	v_mul_f32_e32 v0, v3, v4
	v_mul_f32_e32 v1, v5, v6
	s_nop 1
	v_add_f32_dpp v0, v0, v0 quad_perm:[1,0,3,2] row_mask:0xf bank_mask:0xf
	v_add_f32_dpp v1, v1, v1 quad_perm:[1,0,3,2] row_mask:0xf bank_mask:0xf
	s_nop 1
	v_add_f32_dpp v0, v0, v0 quad_perm:[2,3,0,1] row_mask:0xf bank_mask:0xf
	v_add_f32_dpp v1, v1, v1 quad_perm:[2,3,0,1] row_mask:0xf bank_mask:0xf
	s_nop 1
	v_add_f32_dpp v0, v0, v0 row_half_mirror row_mask:0xf bank_mask:0xf
	v_add_f32_dpp v1, v1, v1 row_half_mirror row_mask:0xf bank_mask:0xf
	s_nop 1
	v_add_f32_dpp v0, v0, v0 row_mirror row_mask:0xf bank_mask:0xf
	v_add_f32_dpp v1, v1, v1 row_mirror row_mask:0xf bank_mask:0xf
	v_mov_b32_e32 v3, v0
	v_mov_b32_e32 v4, v1
	s_nop 1
	v_permlane16_swap_b32_e32 v0, v3
	v_permlane16_swap_b32_e32 v1, v4
	v_add_f32_e32 v0, v0, v3
	v_add_f32_e32 v1, v1, v4
	v_mov_b32_e32 v3, v0
	v_mov_b32_e32 v4, v1
	s_nop 1
	v_permlane32_swap_b32_e32 v0, v3
	v_permlane32_swap_b32_e32 v1, v4
	v_add_f32_e32 v0, v0, v3
	v_add_f32_e32 v1, v1, v4
	s_load_dwordx8 s[36:43], s[92:93], 0x110
	s_cmpk_gt_i32 s21, 0xff
	s_cbranch_scc1 .LBB0_584
	v_cvt_f32_i32_e32 v2, s4
	v_mul_f32_e32 v0, 0x3fb8aa3b, v0
	v_mul_f32_e32 v1, 0x3fb8aa3b, v1
	v_exp_f32_e32 v0, v0
	v_mul_f32_e32 v2, 0xbe99999a, v2
	v_mul_f32_e32 v2, 0x3fb8aa3b, v2
	v_exp_f32_e32 v1, v1
	v_exp_f32_e32 v2, v2
	s_movk_i32 s5, 0x5a
	s_load_dwordx2 s[8:9], s[2:3], 0x40
	v_sub_f32_e32 v0, v0, v1
	v_mov_b32_e32 v1, 0x3f4ccccd
	v_fmamk_f32 v1, v2, 0xbf19999a, v1
	v_add_f32_e32 v232, v1, v0
	v_add_u32_e32 v0, 0xffffff40, v231
	v_sub_u32_e32 v2, 0xc0, v231
	v_max_i32_e32 v0, v0, v2
	v_cmp_lt_u32_e32 vcc, 11, v0
	s_add_u32 s23, s6, 0x8d00000
	s_addc_u32 s24, s7, 0
	v_cndmask_b32_e64 v2, 8, 9, vcc
	v_cmp_lt_u32_e32 vcc, 15, v0
	s_movk_i32 s0, 0x100
	v_cmp_gt_i32_e64 s[0:1], s0, v231
	v_cndmask_b32_e64 v3, 0, 1, vcc
	v_cmp_lt_u32_e32 vcc, 22, v0
	v_sub_f32_e32 v233, 1.0, v1
	s_nop 0
	v_addc_co_u32_e32 v2, vcc, v2, v3, vcc
	v_cmp_lt_u32_e32 vcc, 31, v0
	s_nop 1
	v_cndmask_b32_e64 v3, 0, 1, vcc
	v_cmp_lt_u32_e32 vcc, 45, v0
	s_nop 1
	v_addc_co_u32_e32 v2, vcc, v2, v3, vcc
	v_cmp_lt_u32_e32 vcc, 63, v0
	s_nop 1
	v_cndmask_b32_e64 v3, 0, 1, vcc
	v_cmp_lt_u32_e32 vcc, s5, v0
	s_movk_i32 s5, 0xc0
	s_nop 0
	v_addc_co_u32_e32 v2, vcc, v2, v3, vcc
	v_cmp_lt_i32_e32 vcc, s5, v231
	s_ashr_i32 s5, s4, 31
	s_lshl_b64 s[4:5], s[4:5], 9
	s_waitcnt lgkmcnt(0)
	s_add_u32 s4, s8, s4
	s_addc_u32 s5, s9, s5
	s_add_u32 s25, s6, 0x8d68400
	v_cndmask_b32_e64 v3, 0, 16, vcc
	v_cmp_gt_u32_e32 vcc, 8, v0
	s_addc_u32 s26, s7, 0
	s_lshl_b32 s27, s21, 7
	s_lshl_b32 s28, s22, 7
	v_cndmask_b32_e32 v0, v2, v0, vcc
	s_add_u32 s29, s6, 0x8d68800
	v_add_lshl_u32 v234, v0, v3, 2
	s_addc_u32 s30, s7, 0
	s_branch .LBB0_560
